# S5: S4 + K1 unit remap so the two blocks sharing a CU (i, 256+i) process the same gh (W slice reuse)
# speedup vs baseline: 1.0017x; 1.0017x over previous
_Z12gemm1_kernelPKfS0_S0_PDv8_DF16_PDF16_S3_:
	s_and_b32 s3, s2, 7
	s_ashr_i32 s2, s2, 3
	s_sub_i32 s12, s2, 24
	s_cmp_lt_u32 s12, 4
	s_cselect_b32 s13, 8, 0
	s_sub_i32 s12, s2, 32
	s_cmp_lt_u32 s12, 4
	s_cselect_b32 s12, -8, 0
	s_add_i32 s2, s2, s13
	s_add_i32 s2, s2, s12
	s_mul_hi_i32 s8, s2, 0x2aaaaaab
	s_lshr_b32 s9, s8, 31
	s_ashr_i32 s8, s8, 1
	s_mul_i32 s3, s3, 3
	s_add_i32 s8, s8, s9
	s_load_dwordx4 s[4:7], s[0:1], 0x0
	s_load_dwordx2 s[10:11], s[0:1], 0x10
	s_add_i32 s3, s3, s8
	s_mul_i32 s8, s8, 12
	v_bfe_u32 v85, v0, 6, 2
	s_sub_i32 s8, s2, s8
	v_lshlrev_b32_e32 v1, 5, v85
	s_ashr_i32 s9, s8, 31
	v_lshl_or_b32 v1, s3, 7, v1
	s_lshl_b64 s[2:3], s[8:9], 17
	v_bfe_u32 v18, v0, 3, 3
	v_lshlrev_b32_e32 v4, 5, v0
	v_and_b32_e32 v6, 0x100, v0
	v_or_b32_e32 v2, v1, v18
	s_waitcnt lgkmcnt(0)
	s_add_u32 s2, s6, s2
	v_and_b32_e32 v4, 0x1800, v4
	v_and_b32_e32 v84, 63, v0
	v_mov_b32_e32 v67, 0
	v_ashrrev_i32_e32 v3, 31, v2
	s_addc_u32 s3, s7, s3
	v_lshl_or_b32 v66, v6, 8, v4
	v_lshlrev_b64 v[2:3], 11, v[2:3]
	v_lshl_add_u64 v[4:5], s[2:3], 0, v[66:67]
	v_lshlrev_b32_e32 v66, 2, v84
	v_and_b32_e32 v78, 7, v0
	v_lshl_add_u64 v[68:69], v[4:5], 0, v[66:67]
	v_lshl_add_u64 v[2:3], s[4:5], 0, v[2:3]
	v_lshlrev_b32_e32 v4, 2, v6
	v_mov_b32_e32 v5, v67
	v_lshl_add_u64 v[2:3], v[2:3], 0, v[4:5]
	v_lshlrev_b32_e32 v4, 4, v78
	v_lshl_add_u64 v[70:71], v[2:3], 0, v[4:5]
	s_movk_i32 s4, 0x4000
	v_add_co_u32_e32 v72, vcc, s4, v70
	global_load_dwordx4 v[2:5], v[70:71], off
	s_nop 0
	v_addc_co_u32_e32 v73, vcc, 0, v71, vcc
	global_load_dwordx4 v[6:9], v[72:73], off
	s_mov_b32 s3, 0x8000
	global_load_dword v20, v[68:69], off
	global_load_dword v21, v[68:69], off offset:1792
	global_load_dword v22, v[68:69], off offset:1536
	global_load_dword v23, v[68:69], off offset:1280
	global_load_dword v24, v[68:69], off offset:1024
	global_load_dword v25, v[68:69], off offset:768
	global_load_dword v26, v[68:69], off offset:512
	global_load_dword v27, v[68:69], off offset:256
	v_add_co_u32_e32 v76, vcc, s3, v70
	v_and_b32_e32 v79, 31, v0
	s_nop 0
	v_addc_co_u32_e32 v77, vcc, 0, v71, vcc
	global_load_dwordx4 v[10:13], v[76:77], off
	s_mov_b32 s2, 0xc000
	v_lshrrev_b32_e32 v19, 6, v0
	v_mul_u32_u24_e32 v29, 0x50, v18
	v_lshl_or_b32 v18, s8, 7, v79
	v_add_co_u32_e32 v74, vcc, s2, v70
	v_mul_u32_u24_e32 v28, 0x1400, v19
	v_ashrrev_i32_e32 v19, 31, v18
	v_addc_co_u32_e32 v75, vcc, 0, v71, vcc
	v_lshl_add_u64 v[18:19], v[18:19], 2, s[10:11]
	global_load_dwordx4 v[14:17], v[74:75], off
	global_load_dword v80, v[18:19], off
	global_load_dword v83, v[18:19], off offset:128
	global_load_dword v81, v[18:19], off offset:256
	global_load_dword v82, v[18:19], off offset:384
	v_lshrrev_b32_e32 v86, 8, v0
	v_mov_b32_e32 v18, 0xa000
	s_movk_i32 s5, 0x2000
	v_lshl_add_u32 v32, v86, 13, v18
	v_add_co_u32_e32 v18, vcc, s5, v68
	global_load_dwordx4 v[62:65], v[70:71], off offset:128
	global_load_dwordx4 v[58:61], v[72:73], off offset:128
	global_load_dwordx4 v[54:57], v[76:77], off offset:128
	global_load_dwordx4 v[50:53], v[74:75], off offset:128
	v_addc_co_u32_e32 v19, vcc, 0, v69, vcc
	global_load_dword v91, v[18:19], off offset:1792
	global_load_dword v104, v[18:19], off offset:1536
	global_load_dword v105, v[18:19], off offset:1280
	global_load_dword v106, v[18:19], off offset:1024
	global_load_dword v107, v[18:19], off offset:768
	global_load_dword v108, v[18:19], off offset:512
	global_load_dword v109, v[18:19], off offset:256
	global_load_dword v110, v[18:19], off
	v_bfe_u32 v67, v0, 5, 1
	v_mul_u32_u24_e32 v30, 0x50, v79
	v_lshlrev_b32_e32 v31, 4, v67
	v_add3_u32 v89, v28, v30, v31
	v_lshl_or_b32 v88, v84, 4, v32
	s_waitcnt vmcnt(18)
	v_mov_b32_e32 v33, v3
	v_mov_b32_e32 v3, v5
	v_lshlrev_b32_e32 v5, 4, v0
	v_mov_b32_e32 v19, v8
	v_cvt_pk_f16_f32 v8, v20, v27
	v_and_b32_e32 v5, 0x800, v5
	v_lshlrev_b32_e32 v20, 10, v67
	v_or3_b32 v5, v32, v5, v20
	v_lshlrev_b32_e32 v20, 3, v0
	v_mov_b32_e32 v18, v9
	s_waitcnt vmcnt(17)
	v_mov_b32_e32 v35, v11
	v_cvt_pk_f16_f32 v11, v22, v21
	v_and_b32_e32 v20, 0x200, v20
	v_lshlrev_b32_e32 v21, 4, v79
	v_or3_b32 v87, v5, v20, v21
	v_or_b32_e32 v5, v28, v29
	v_mov_b32_e32 v34, v10
	v_cvt_pk_f16_f32 v10, v24, v23
	v_cvt_pk_f16_f32 v9, v26, v25
	v_lshl_add_u32 v90, v78, 3, v5
	v_cvt_pk_f16_f32 v3, v4, v3
	v_cvt_pk_f16_f32 v2, v2, v33
	v_cvt_pk_f16_f32 v5, v19, v18
	v_cvt_pk_f16_f32 v4, v6, v7
	s_waitcnt vmcnt(16)
	ds_write_b128 v87, v[8:11]
	ds_write2_b64 v90, v[2:3], v[4:5] offset1:80
	v_cvt_pk_f16_f32 v3, v12, v13
	v_cvt_pk_f16_f32 v2, v34, v35
	v_cvt_pk_f16_f32 v5, v16, v17
	v_cvt_pk_f16_f32 v4, v14, v15
	ds_write2_b64 v90, v[2:3], v[4:5] offset0:160 offset1:240
	v_add_co_u32_e32 v2, vcc, s4, v68
	global_load_dwordx4 v[34:37], v[70:71], off offset:256
	global_load_dwordx4 v[38:41], v[72:73], off offset:256
	global_load_dwordx4 v[42:45], v[76:77], off offset:256
	global_load_dwordx4 v[46:49], v[74:75], off offset:256
	v_addc_co_u32_e32 v3, vcc, 0, v69, vcc
	global_load_dword v111, v[2:3], off offset:1792
	global_load_dword v112, v[2:3], off offset:1536
	global_load_dword v113, v[2:3], off offset:1280
	global_load_dword v114, v[2:3], off offset:1024
	global_load_dword v115, v[2:3], off offset:768
	global_load_dword v116, v[2:3], off offset:512
	global_load_dword v117, v[2:3], off offset:256
	global_load_dword v118, v[2:3], off
	s_waitcnt lgkmcnt(0)
	s_barrier
	ds_read_b128 v[2:5], v89
	ds_read_b128 v[6:9], v88
	ds_read_b128 v[92:95], v89 offset:32
	ds_read_b128 v[10:13], v88 offset:1024
	s_waitcnt lgkmcnt(2)
	v_mfma_f32_32x32x16_f16 v[18:33], v[2:5], v[6:9], 0
	ds_read_b128 v[96:99], v88 offset:2048
	ds_read_b128 v[100:103], v88 offset:3072
	s_waitcnt vmcnt(12)
	s_movk_i32 s4, 0x6000
	s_waitcnt lgkmcnt(2)
	v_mfma_f32_32x32x16_f16 v[2:17], v[2:5], v[10:13], 0
	s_waitcnt lgkmcnt(1)
	v_mfma_f32_32x32x16_f16 v[18:33], v[92:95], v[96:99], v[18:33]
	v_mov_b32_e32 v96, v53
	v_mov_b32_e32 v97, v56
	v_mov_b32_e32 v98, v52
	v_mov_b32_e32 v99, v57
	s_waitcnt lgkmcnt(0)
	v_mfma_f32_32x32x16_f16 v[2:17], v[92:95], v[100:103], v[2:17]
	v_mov_b32_e32 v92, v60
	v_mov_b32_e32 v93, v63
	v_mov_b32_e32 v94, v62
	v_mov_b32_e32 v95, v61
	v_cvt_pk_f16_f32 v63, v104, v91
	v_cvt_pk_f16_f32 v62, v106, v105
	v_cvt_pk_f16_f32 v61, v108, v107
	v_cvt_pk_f16_f32 v60, v110, v109
	v_cvt_pk_f16_f32 v53, v64, v65
	v_cvt_pk_f16_f32 v52, v94, v93
	v_cvt_pk_f16_f32 v57, v92, v95
	v_cvt_pk_f16_f32 v56, v58, v59
	v_add_u32_e32 v91, 0x800, v90
	ds_write_b128 v87, v[60:63] offset:4096
	ds_write2_b64 v91, v[52:53], v[56:57] offset0:64 offset1:144
	v_cvt_pk_f16_f32 v53, v97, v99
	v_cvt_pk_f16_f32 v52, v54, v55
	v_cvt_pk_f16_f32 v55, v98, v96
	v_cvt_pk_f16_f32 v54, v50, v51
	v_add_u32_e32 v92, 0xc00, v90
	v_add_co_u32_e32 v94, vcc, s4, v68
	ds_write2_b64 v92, v[52:53], v[54:55] offset0:96 offset1:176
	s_nop 0
	v_addc_co_u32_e32 v95, vcc, 0, v69, vcc
	global_load_dwordx4 v[50:53], v[70:71], off offset:384
	global_load_dwordx4 v[54:57], v[72:73], off offset:384
	global_load_dwordx4 v[58:61], v[76:77], off offset:384
	global_load_dwordx4 v[62:65], v[74:75], off offset:384
	global_load_dword v93, v[94:95], off offset:1792
	global_load_dword v110, v[94:95], off offset:1536
	global_load_dword v119, v[94:95], off offset:1280
	global_load_dword v120, v[94:95], off offset:1024
	global_load_dword v121, v[94:95], off offset:768
	global_load_dword v122, v[94:95], off offset:512
	global_load_dword v123, v[94:95], off offset:256
	global_load_dword v124, v[94:95], off
	s_waitcnt lgkmcnt(0)
	s_barrier
	ds_read_b128 v[94:97], v89 offset:2560
	ds_read_b128 v[98:101], v88 offset:4096
	ds_read_b128 v[102:105], v89 offset:2592
	ds_read_b128 v[106:109], v88 offset:5120
	s_waitcnt lgkmcnt(2)
	v_mfma_f32_32x32x16_f16 v[18:33], v[94:97], v[98:101], v[18:33]
	s_waitcnt lgkmcnt(0)
	v_mfma_f32_32x32x16_f16 v[2:17], v[94:97], v[106:109], v[2:17]
	ds_read_b128 v[94:97], v88 offset:6144
	ds_read_b128 v[98:101], v88 offset:7168
	s_waitcnt vmcnt(12)
	s_waitcnt lgkmcnt(1)
	v_mfma_f32_32x32x16_f16 v[18:33], v[102:105], v[94:97], v[18:33]
	v_mov_b32_e32 v94, v37
	v_mov_b32_e32 v95, v39
	v_mov_b32_e32 v96, v36
	v_mov_b32_e32 v97, v38
	v_cvt_pk_f16_f32 v39, v112, v111
	v_cvt_pk_f16_f32 v38, v114, v113
	v_cvt_pk_f16_f32 v37, v116, v115
	v_cvt_pk_f16_f32 v36, v118, v117
	ds_write_b128 v87, v[36:39]
	v_cvt_pk_f16_f32 v37, v96, v94
	v_cvt_pk_f16_f32 v36, v34, v35
	v_cvt_pk_f16_f32 v35, v40, v41
	v_cvt_pk_f16_f32 v34, v97, v95
	ds_write2_b64 v90, v[36:37], v[34:35] offset1:80
	v_cvt_pk_f16_f32 v35, v44, v45
	v_cvt_pk_f16_f32 v34, v42, v43
	v_cvt_pk_f16_f32 v37, v48, v49
	v_cvt_pk_f16_f32 v36, v46, v47
	v_add_co_u32_e32 v94, vcc, s3, v68
	s_waitcnt lgkmcnt(2)
	v_mfma_f32_32x32x16_f16 v[2:17], v[102:105], v[98:101], v[2:17]
	ds_write2_b64 v90, v[34:35], v[36:37] offset0:160 offset1:240
	v_addc_co_u32_e32 v95, vcc, 0, v69, vcc
	global_load_dwordx4 v[34:37], v[70:71], off offset:512
	global_load_dwordx4 v[38:41], v[72:73], off offset:512
	global_load_dwordx4 v[42:45], v[76:77], off offset:512
	global_load_dwordx4 v[46:49], v[74:75], off offset:512
	global_load_dword v111, v[94:95], off offset:1792
	global_load_dword v112, v[94:95], off offset:1536
	global_load_dword v113, v[94:95], off offset:1280
	global_load_dword v114, v[94:95], off offset:1024
	global_load_dword v115, v[94:95], off offset:768
	global_load_dword v116, v[94:95], off offset:512
	global_load_dword v117, v[94:95], off offset:256
	global_load_dword v118, v[94:95], off
	s_waitcnt lgkmcnt(0)
	s_barrier
	ds_read_b128 v[94:97], v89
	ds_read_b128 v[98:101], v88
	ds_read_b128 v[102:105], v89 offset:32
	ds_read_b128 v[106:109], v88 offset:1024
	s_waitcnt lgkmcnt(2)
	v_mfma_f32_32x32x16_f16 v[18:33], v[94:97], v[98:101], v[18:33]
	s_mov_b32 s3, 0xa000
	s_waitcnt lgkmcnt(0)
	v_mfma_f32_32x32x16_f16 v[2:17], v[94:97], v[106:109], v[2:17]
	ds_read_b128 v[94:97], v88 offset:2048
	ds_read_b128 v[98:101], v88 offset:3072
	s_waitcnt vmcnt(12)
	s_waitcnt lgkmcnt(1)
	v_mfma_f32_32x32x16_f16 v[18:33], v[102:105], v[94:97], v[18:33]
	v_mov_b32_e32 v94, v51
	v_mov_b32_e32 v95, v61
	v_mov_b32_e32 v96, v63
	v_mov_b32_e32 v97, v60
	v_cvt_pk_f16_f32 v63, v110, v93
	v_cvt_pk_f16_f32 v61, v122, v121
	s_waitcnt lgkmcnt(0)
	v_mfma_f32_32x32x16_f16 v[2:17], v[102:105], v[98:101], v[2:17]
	v_mov_b32_e32 v98, v62
	v_cvt_pk_f16_f32 v62, v120, v119
	v_cvt_pk_f16_f32 v60, v124, v123
	v_cvt_pk_f16_f32 v51, v52, v53
	v_cvt_pk_f16_f32 v50, v50, v94
	v_cvt_pk_f16_f32 v53, v56, v57
	v_cvt_pk_f16_f32 v52, v54, v55
	ds_write_b128 v87, v[60:63] offset:4096
	ds_write2_b64 v91, v[50:51], v[52:53] offset0:64 offset1:144
	v_cvt_pk_f16_f32 v51, v97, v95
	v_cvt_pk_f16_f32 v50, v58, v59
	v_cvt_pk_f16_f32 v53, v64, v65
	v_cvt_pk_f16_f32 v52, v98, v96
	v_add_co_u32_e32 v94, vcc, s3, v68
	ds_write2_b64 v92, v[50:51], v[52:53] offset0:96 offset1:176
	s_nop 0
	v_addc_co_u32_e32 v95, vcc, 0, v69, vcc
	global_load_dwordx4 v[50:53], v[70:71], off offset:640
	global_load_dwordx4 v[54:57], v[72:73], off offset:640
	global_load_dwordx4 v[58:61], v[76:77], off offset:640
	global_load_dwordx4 v[62:65], v[74:75], off offset:640
	global_load_dword v93, v[94:95], off offset:1792
	global_load_dword v110, v[94:95], off offset:1536
	global_load_dword v119, v[94:95], off offset:1280
	global_load_dword v120, v[94:95], off offset:1024
	global_load_dword v121, v[94:95], off offset:768
	global_load_dword v122, v[94:95], off offset:512
	global_load_dword v123, v[94:95], off offset:256
	global_load_dword v124, v[94:95], off
	s_waitcnt lgkmcnt(0)
	s_barrier
	ds_read_b128 v[94:97], v89 offset:2560
	ds_read_b128 v[98:101], v88 offset:4096
	ds_read_b128 v[102:105], v89 offset:2592
	ds_read_b128 v[106:109], v88 offset:5120
	s_waitcnt lgkmcnt(2)
	v_mfma_f32_32x32x16_f16 v[18:33], v[94:97], v[98:101], v[18:33]
	s_waitcnt lgkmcnt(0)
	v_mfma_f32_32x32x16_f16 v[2:17], v[94:97], v[106:109], v[2:17]
	ds_read_b128 v[94:97], v88 offset:6144
	ds_read_b128 v[98:101], v88 offset:7168
	s_waitcnt vmcnt(12)
	s_waitcnt lgkmcnt(1)
	v_mfma_f32_32x32x16_f16 v[18:33], v[102:105], v[94:97], v[18:33]
	v_mov_b32_e32 v94, v41
	v_mov_b32_e32 v95, v40
	v_mov_b32_e32 v96, v35
	v_mov_b32_e32 v35, v37
	v_mov_b32_e32 v97, v42
	v_cvt_pk_f16_f32 v42, v114, v113
	s_waitcnt lgkmcnt(0)
	v_mfma_f32_32x32x16_f16 v[2:17], v[102:105], v[98:101], v[2:17]
	v_mov_b32_e32 v98, v43
	v_cvt_pk_f16_f32 v43, v112, v111
	v_cvt_pk_f16_f32 v41, v116, v115
	v_cvt_pk_f16_f32 v40, v118, v117
	v_cvt_pk_f16_f32 v35, v36, v35
	v_cvt_pk_f16_f32 v34, v34, v96
	v_cvt_pk_f16_f32 v37, v95, v94
	v_cvt_pk_f16_f32 v36, v38, v39
	ds_write_b128 v87, v[40:43]
	ds_write2_b64 v90, v[34:35], v[36:37] offset1:80
	v_cvt_pk_f16_f32 v35, v44, v45
	v_cvt_pk_f16_f32 v34, v97, v98
	v_cvt_pk_f16_f32 v37, v48, v49
	v_cvt_pk_f16_f32 v36, v46, v47
	v_add_co_u32_e32 v94, vcc, s2, v68
	ds_write2_b64 v90, v[34:35], v[36:37] offset0:160 offset1:240
	s_nop 0
	v_addc_co_u32_e32 v95, vcc, 0, v69, vcc
	global_load_dwordx4 v[34:37], v[70:71], off offset:768
	global_load_dwordx4 v[38:41], v[72:73], off offset:768
	global_load_dwordx4 v[42:45], v[76:77], off offset:768
	global_load_dwordx4 v[46:49], v[74:75], off offset:768
	global_load_dword v111, v[94:95], off offset:1792
	global_load_dword v112, v[94:95], off offset:1536
	global_load_dword v113, v[94:95], off offset:1280
	global_load_dword v114, v[94:95], off offset:1024
	global_load_dword v115, v[94:95], off offset:768
	global_load_dword v116, v[94:95], off offset:512
	global_load_dword v117, v[94:95], off offset:256
	global_load_dword v118, v[94:95], off
	s_waitcnt lgkmcnt(0)
	s_barrier
	ds_read_b128 v[94:97], v89
	ds_read_b128 v[98:101], v88
	ds_read_b128 v[102:105], v89 offset:32
	ds_read_b128 v[106:109], v88 offset:1024
	s_waitcnt lgkmcnt(0)
	v_mfma_f32_32x32x16_f16 v[2:17], v[94:97], v[106:109], v[2:17]
	s_mov_b32 s2, 0xe000
	v_add_co_u32_e32 v68, vcc, s2, v68
	v_cmp_eq_u32_e64 s[2:3], 1, v86
	s_nop 0
	v_addc_co_u32_e32 v69, vcc, 0, v69, vcc
	v_cmp_ne_u32_e32 vcc, 1, v86
	v_mfma_f32_32x32x16_f16 v[18:33], v[94:97], v[98:101], v[18:33]
	ds_read_b128 v[94:97], v88 offset:2048
	ds_read_b128 v[98:101], v88 offset:3072
	s_waitcnt vmcnt(12)
	s_waitcnt lgkmcnt(0)
	v_mfma_f32_32x32x16_f16 v[2:17], v[102:105], v[98:101], v[2:17]
	v_mov_b32_e32 v98, v51
	v_mov_b32_e32 v51, v53
	v_mov_b32_e32 v53, v57
	v_mov_b32_e32 v57, v65
	v_cvt_pk_f16_f32 v51, v52, v51
	v_cvt_pk_f16_f32 v50, v50, v98
	v_mfma_f32_32x32x16_f16 v[18:33], v[102:105], v[94:97], v[18:33]
	v_cvt_pk_f16_f32 v97, v110, v93
	v_cvt_pk_f16_f32 v96, v120, v119
	v_cvt_pk_f16_f32 v95, v122, v121
	v_cvt_pk_f16_f32 v94, v124, v123
	v_cvt_pk_f16_f32 v53, v56, v53
	v_cvt_pk_f16_f32 v52, v54, v55
	ds_write_b128 v87, v[94:97] offset:4096
	ds_write2_b64 v91, v[50:51], v[52:53] offset0:64 offset1:144
	v_cvt_pk_f16_f32 v51, v60, v61
	v_cvt_pk_f16_f32 v50, v58, v59
	v_cvt_pk_f16_f32 v53, v64, v57
	v_cvt_pk_f16_f32 v52, v62, v63
	ds_write2_b64 v92, v[50:51], v[52:53] offset0:96 offset1:176
	global_load_dwordx4 v[50:53], v[70:71], off offset:896
	global_load_dwordx4 v[54:57], v[72:73], off offset:896
	global_load_dwordx4 v[58:61], v[76:77], off offset:896
	global_load_dwordx4 v[62:65], v[74:75], off offset:896
	s_nop 0
	global_load_dword v76, v[68:69], off offset:1792
	global_load_dword v77, v[68:69], off offset:1536
	global_load_dword v93, v[68:69], off offset:1280
	global_load_dword v102, v[68:69], off offset:1024
	global_load_dword v103, v[68:69], off offset:768
	global_load_dword v104, v[68:69], off offset:512
	global_load_dword v105, v[68:69], off offset:256
	global_load_dword v106, v[68:69], off
	s_waitcnt lgkmcnt(0)
	s_barrier
	ds_read_b128 v[68:71], v89 offset:2560
	ds_read_b128 v[72:75], v88 offset:4096
	ds_read_b128 v[94:97], v89 offset:2592
	ds_read_b128 v[98:101], v88 offset:5120
	s_waitcnt lgkmcnt(2)
	v_mfma_f32_32x32x16_f16 v[18:33], v[68:71], v[72:75], v[18:33]
	s_waitcnt lgkmcnt(0)
	v_mfma_f32_32x32x16_f16 v[2:17], v[68:71], v[98:101], v[2:17]
	ds_read_b128 v[68:71], v88 offset:6144
	ds_read_b128 v[72:75], v88 offset:7168
	s_waitcnt vmcnt(12)
	s_waitcnt lgkmcnt(1)
	v_mfma_f32_32x32x16_f16 v[18:33], v[94:97], v[68:71], v[18:33]
	v_mov_b32_e32 v68, v37
	v_mov_b32_e32 v69, v39
	v_mov_b32_e32 v70, v36
	v_mov_b32_e32 v71, v38
	v_cvt_pk_f16_f32 v39, v112, v111
	v_cvt_pk_f16_f32 v38, v114, v113
	s_waitcnt lgkmcnt(0)
	v_mfma_f32_32x32x16_f16 v[2:17], v[94:97], v[72:75], v[2:17]
	v_cvt_pk_f16_f32 v37, v116, v115
	v_cvt_pk_f16_f32 v36, v118, v117
	ds_write_b128 v87, v[36:39]
	v_cvt_pk_f16_f32 v37, v70, v68
	v_cvt_pk_f16_f32 v36, v34, v35
	v_cvt_pk_f16_f32 v35, v40, v41
	v_cvt_pk_f16_f32 v34, v71, v69
	ds_write2_b64 v90, v[36:37], v[34:35] offset1:80
	v_cvt_pk_f16_f32 v35, v44, v45
	v_cvt_pk_f16_f32 v34, v42, v43
	v_cvt_pk_f16_f32 v37, v48, v49
	v_cvt_pk_f16_f32 v36, v46, v47
	ds_write2_b64 v90, v[34:35], v[36:37] offset0:160 offset1:240
	s_waitcnt lgkmcnt(0)
	s_barrier
	ds_read_b128 v[34:37], v89
	ds_read_b128 v[38:41], v88
	ds_read_b128 v[42:45], v89 offset:32
	ds_read_b128 v[46:49], v88 offset:1024
	s_waitcnt lgkmcnt(2)
	v_mfma_f32_32x32x16_f16 v[18:33], v[34:37], v[38:41], v[18:33]
	s_waitcnt lgkmcnt(0)
	v_mfma_f32_32x32x16_f16 v[2:17], v[34:37], v[46:49], v[2:17]
	ds_read_b128 v[34:37], v88 offset:2048
	ds_read_b128 v[38:41], v88 offset:3072
	s_waitcnt vmcnt(0)
	s_waitcnt lgkmcnt(1)
	v_mfma_f32_32x32x16_f16 v[18:33], v[42:45], v[34:37], v[18:33]
	v_mov_b32_e32 v46, v58
	v_mov_b32_e32 v47, v65
	v_mov_b32_e32 v48, v60
	v_mov_b32_e32 v49, v62
	v_cvt_pk_f16_f32 v37, v77, v76
	v_cvt_pk_f16_f32 v36, v102, v93
	v_cvt_pk_f16_f32 v35, v104, v103
	s_waitcnt lgkmcnt(0)
	v_mfma_f32_32x32x16_f16 v[2:17], v[42:45], v[38:41], v[2:17]
	v_mov_b32_e32 v38, v50
	v_mov_b32_e32 v39, v57
	v_mov_b32_e32 v40, v52
	v_mov_b32_e32 v41, v54
	v_mov_b32_e32 v42, v56
	v_mov_b32_e32 v43, v51
	v_mov_b32_e32 v44, v61
	v_mov_b32_e32 v45, v63
	v_cvt_pk_f16_f32 v34, v106, v105
	ds_write_b128 v87, v[34:37] offset:4096
	v_cvt_pk_f16_f32 v35, v40, v53
	v_cvt_pk_f16_f32 v34, v38, v43
	v_cvt_pk_f16_f32 v37, v42, v39
	v_cvt_pk_f16_f32 v36, v41, v55
	ds_write2_b64 v91, v[34:35], v[36:37] offset0:64 offset1:144
	v_cvt_pk_f16_f32 v35, v48, v44
	v_cvt_pk_f16_f32 v34, v46, v59
	v_cvt_pk_f16_f32 v37, v64, v47
	v_cvt_pk_f16_f32 v36, v49, v45
	ds_write2_b64 v92, v[34:35], v[36:37] offset0:96 offset1:176
	s_waitcnt lgkmcnt(0)
	s_barrier
	ds_read_b128 v[34:37], v89 offset:2560
	ds_read_b128 v[38:41], v88 offset:4096
	ds_read_b128 v[42:45], v89 offset:2592
	ds_read_b128 v[46:49], v88 offset:5120
	s_waitcnt lgkmcnt(2)
	v_mfma_f32_32x32x16_f16 v[18:33], v[34:37], v[38:41], v[18:33]
	s_waitcnt lgkmcnt(0)
	v_mfma_f32_32x32x16_f16 v[2:17], v[34:37], v[46:49], v[2:17]
	ds_read_b128 v[34:37], v88 offset:6144
	ds_read_b128 v[38:41], v88 offset:7168
	s_waitcnt lgkmcnt(0)
	s_barrier
	v_mfma_f32_32x32x16_f16 v[18:33], v[42:45], v[34:37], v[18:33]
	v_mfma_f32_32x32x16_f16 v[2:17], v[42:45], v[38:41], v[2:17]
	s_and_saveexec_b64 s[4:5], s[2:3]
	s_cbranch_execz .LBB0_2
	v_lshl_or_b32 v34, v85, 13, v66
	s_nop 7
	ds_write2st64_b32 v34, v18, v19 offset1:1
	ds_write2st64_b32 v34, v20, v21 offset0:2 offset1:3
	ds_write2st64_b32 v34, v22, v23 offset0:4 offset1:5
	ds_write2st64_b32 v34, v24, v25 offset0:6 offset1:7
	ds_write2st64_b32 v34, v26, v27 offset0:8 offset1:9
	ds_write2st64_b32 v34, v28, v29 offset0:10 offset1:11
	ds_write2st64_b32 v34, v30, v31 offset0:12 offset1:13
	ds_write2st64_b32 v34, v32, v33 offset0:14 offset1:15
	ds_write2st64_b32 v34, v2, v3 offset0:16 offset1:17
	ds_write2st64_b32 v34, v4, v5 offset0:18 offset1:19
	ds_write2st64_b32 v34, v6, v7 offset0:20 offset1:21
	ds_write2st64_b32 v34, v8, v9 offset0:22 offset1:23
	ds_write2st64_b32 v34, v10, v11 offset0:24 offset1:25
	ds_write2st64_b32 v34, v12, v13 offset0:26 offset1:27
	ds_write2st64_b32 v34, v14, v15 offset0:28 offset1:29
	ds_write2st64_b32 v34, v16, v17 offset0:30 offset1:31
